# vmcnt
# speedup vs baseline: 1.0075x; 1.0004x over previous
.Lpr2_nowrite:
	s_movk_i32 s4, 0x1a0
	v_add_u32_e32 v59, s29, v69
	v_cmp_gt_u32_e32 vcc, s4, v59
	v_add_f32_e32 v50, v78, v79
	v_lshlrev_b32_e32 v18, 2, v59
	s_and_saveexec_b64 s[0:1], vcc
	v_fma_f32 v50, v76, v50, -v77
	ds_write_b32 v18, v50 offset:41984
	s_or_b64 exec, exec, s[0:1]
	s_mov_b64 s[14:15], s[58:59]
	s_waitcnt lgkmcnt(0)
	v_mov_b32_e32 v18, 0xbfb8aa3b
	s_lshl_b32 s3, s21, 4
	s_cmpk_gt_i32 s20, 0x7fff
	v_cmp_gt_u32_e32 vcc, 32, v69
	s_waitcnt lgkmcnt(0)
	v_mul_f32_e32 v18, s34, v18
	v_exp_f32_e32 v70, v18
	v_mov_b32_e32 v18, 0
	v_and_b32_e32 v71, 48, v0
	s_mov_b32 s10, s20
	s_barrier
	s_cbranch_scc1 .LBB0_37
	s_sub_i32 s2, s20, s3
	s_add_i32 s9, s3, s20
	s_mov_b32 s4, 1.0
	s_mov_b32 s8, 0x3fb4c4be
	v_lshlrev_b32_e32 v72, 4, v69
	v_cmp_eq_u32_e64 s[0:1], 1, v1
	v_lshl_add_u32 v38, s2, 5, v69
	v_lshlrev_b32_e32 v38, 2, v38
	v_lshlrev_b32_e32 v39, 7, v68
	v_lshl_add_u32 v39, v1, 5, v39
	s_lshl_b32 s7, s21, 11
	v_mov_b32_e32 v18, 0
	s_mov_b32 s12, 0
	s_mov_b32 s2, 0x4a000000
	s_mov_b32 s5, s4
	s_mov_b32 s6, 0x3f34c4be
	v_mov_b64_e32 v[40:41], s[8:9]
	s_mov_b32 s8, 0x400a34e2
	s_mov_b32 s33, 0
	s_waitcnt vmcnt(0)
	s_branch .LBB0_35
.LBB0_34:
	s_or_b64 exec, exec, s[10:11]
	ds_read_b128 v[18:21], v72
	s_waitcnt vmcnt(3)
	v_cvt_pk_f16_f32 v14, v14, v15
	v_cvt_pk_f16_f32 v15, v16, v17
	v_cvt_pk_f16_f32 v16, v10, v11
	ds_read_b128 v[22:25], v71 offset:41984
	v_cvt_pk_f16_f32 v17, v12, v13
	ds_read_b128 v[10:13], v72 offset:1024
	ds_read_b128 v[26:29], v71 offset:42048
	s_waitcnt vmcnt(1)
	v_cvt_pk_f16_f32 v0, v6, v7
	v_cvt_pk_f16_f32 v1, v8, v9
	v_cvt_pk_f16_f32 v2, v2, v3
	v_cvt_pk_f16_f32 v3, v4, v5
	s_waitcnt lgkmcnt(2)
	v_mfma_f32_16x16x32_f16 v[30:33], v[18:21], v[14:17], v[22:25]
	s_add_i32 s10, s20, s12
	v_mfma_f32_16x16x32_f16 v[18:21], v[18:21], v[0:3], v[22:25]
	ds_read_b128 v[4:7], v72 offset:2048
	s_nop 1
	ds_read_b128 v[22:25], v71 offset:42112
	s_waitcnt lgkmcnt(2)
	v_mfma_f32_16x16x32_f16 v[34:37], v[10:13], v[14:17], v[26:29]
	v_exp_f32_e32 v78, v30
	v_exp_f32_e32 v79, v31
	v_exp_f32_e32 v20, v20
	v_mfma_f32_16x16x32_f16 v[8:11], v[10:13], v[0:3], v[26:29]
	ds_read_b128 v[44:47], v71 offset:42176
	s_nop 2
	v_exp_f32_e64 v80, v34 clamp
	v_exp_f32_e64 v81, v35 clamp
	ds_read_b128 v[26:29], v72 offset:3072
	s_waitcnt lgkmcnt(2)
	v_mfma_f32_16x16x32_f16 v[48:51], v[4:7], v[14:17], v[22:25]
	v_exp_f32_e64 v82, v36 clamp
	v_exp_f32_e64 v83, v37 clamp
	v_exp_f32_e32 v21, v21
	v_mfma_f32_16x16x32_f16 v[22:25], v[4:7], v[0:3], v[22:25]
	ds_read_b128 v[52:55], v72 offset:4096
	ds_read_b128 v[56:59], v71 offset:42240
	s_nop 1
	v_exp_f32_e32 v4, v48
	s_waitcnt lgkmcnt(2)
	v_mfma_f32_16x16x32_f16 v[60:63], v[26:29], v[14:17], v[44:47]
	v_exp_f32_e32 v5, v49
	v_exp_f32_e32 v48, v32
	v_exp_f32_e32 v49, v33
	v_mfma_f32_16x16x32_f16 v[26:29], v[26:29], v[0:3], v[44:47]
	ds_read_b128 v[64:67], v71 offset:42304
	v_exp_f32_e32 v6, v50
	v_exp_f32_e32 v7, v51
	ds_read_b128 v[44:47], v72 offset:5120
	s_waitcnt lgkmcnt(2)
	v_mfma_f32_16x16x32_f16 v[74:77], v[52:55], v[14:17], v[56:59]
	v_exp_f32_e32 v50, v18
	v_exp_f32_e32 v51, v19
	v_exp_f32_e32 v26, v26
	v_mfma_f32_16x16x32_f16 v[30:33], v[52:55], v[0:3], v[56:59]
	v_exp_f32_e64 v52, v8 clamp
	v_exp_f32_e64 v53, v9 clamp
	v_exp_f32_e32 v8, v22
	s_waitcnt lgkmcnt(0)
	v_mfma_f32_16x16x32_f16 v[34:37], v[44:47], v[14:17], v[64:67]
	v_exp_f32_e32 v9, v23
	v_exp_f32_e64 v22, v10 clamp
	v_exp_f32_e64 v23, v11 clamp
	v_mfma_f32_16x16x32_f16 v[44:47], v[44:47], v[0:3], v[64:67]
	v_exp_f32_e32 v10, v24
	v_exp_f32_e32 v11, v25
	s_nop 1
	v_exp_f32_e32 v12, v34
	v_exp_f32_e32 v13, v35
	v_exp_f32_e32 v18, v36
	v_exp_f32_e32 v24, v60
	v_exp_f32_e32 v25, v61
	v_exp_f32_e64 v54, v74 clamp
	v_exp_f32_e64 v55, v75 clamp
	v_exp_f32_e32 v34, v62
	v_exp_f32_e32 v35, v63
	v_exp_f32_e64 v56, v76 clamp
	v_exp_f32_e64 v57, v77 clamp
	v_exp_f32_e32 v19, v37
	v_exp_f32_e32 v27, v27
	v_exp_f32_e64 v30, v30 clamp
	v_exp_f32_e64 v31, v31 clamp
	v_exp_f32_e32 v36, v44
	v_exp_f32_e32 v37, v45
	v_exp_f32_e32 v28, v28
	v_exp_f32_e32 v29, v29
	v_exp_f32_e64 v32, v32 clamp
	v_exp_f32_e64 v33, v33 clamp
	v_exp_f32_e32 v44, v46
	v_exp_f32_e32 v45, v47
	v_pk_fma_f32 v[58:59], v[80:81], s[2:3], 1.0 op_sel_hi:[1,0,0]
	v_pk_fma_f32 v[60:61], v[82:83], s[2:3], 1.0 op_sel_hi:[1,0,0]
	v_pk_fma_f32 v[52:53], v[52:53], s[2:3], 1.0 op_sel_hi:[1,0,0]
	v_pk_fma_f32 v[22:23], v[22:23], s[2:3], 1.0 op_sel_hi:[1,0,0]
	v_pk_fma_f32 v[54:55], v[54:55], s[2:3], 1.0 op_sel_hi:[1,0,0]
	v_pk_fma_f32 v[56:57], v[56:57], s[2:3], 1.0 op_sel_hi:[1,0,0]
	v_pk_fma_f32 v[30:31], v[30:31], s[2:3], 1.0 op_sel_hi:[1,0,0]
	v_pk_fma_f32 v[32:33], v[32:33], s[2:3], 1.0 op_sel_hi:[1,0,0]
	v_pk_fma_f32 v[46:47], v[78:79], v[58:59], v[58:59]
	v_pk_fma_f32 v[48:49], v[48:49], v[60:61], v[60:61]
	v_pk_fma_f32 v[50:51], v[50:51], v[52:53], v[52:53]
	v_pk_fma_f32 v[20:21], v[20:21], v[22:23], v[22:23]
	v_pk_fma_f32 v[24:25], v[24:25], v[54:55], v[54:55]
	v_pk_fma_f32 v[34:35], v[34:35], v[56:57], v[56:57]
	v_pk_fma_f32 v[26:27], v[26:27], v[30:31], v[30:31]
	v_pk_fma_f32 v[28:29], v[28:29], v[32:33], v[32:33]
	v_pk_fma_f32 v[58:59], v[58:59], s[6:7], v[40:41] op_sel_hi:[1,0,0] neg_lo:[1,0,0] neg_hi:[1,0,0]
	v_pk_fma_f32 v[60:61], v[60:61], s[6:7], v[40:41] op_sel_hi:[1,0,0] neg_lo:[1,0,0] neg_hi:[1,0,0]
	v_pk_fma_f32 v[52:53], v[52:53], s[6:7], v[40:41] op_sel_hi:[1,0,0] neg_lo:[1,0,0] neg_hi:[1,0,0]
	v_pk_fma_f32 v[22:23], v[22:23], s[6:7], v[40:41] op_sel_hi:[1,0,0] neg_lo:[1,0,0] neg_hi:[1,0,0]
	v_pk_fma_f32 v[54:55], v[54:55], s[6:7], v[40:41] op_sel_hi:[1,0,0] neg_lo:[1,0,0] neg_hi:[1,0,0]
	v_pk_fma_f32 v[56:57], v[56:57], s[6:7], v[40:41] op_sel_hi:[1,0,0] neg_lo:[1,0,0] neg_hi:[1,0,0]
	v_pk_fma_f32 v[30:31], v[30:31], s[6:7], v[40:41] op_sel_hi:[1,0,0] neg_lo:[1,0,0] neg_hi:[1,0,0]
	v_pk_fma_f32 v[32:33], v[32:33], s[6:7], v[40:41] op_sel_hi:[1,0,0] neg_lo:[1,0,0] neg_hi:[1,0,0]
	v_pk_fma_f32 v[46:47], v[4:5], v[46:47], v[46:47]
	v_pk_fma_f32 v[48:49], v[6:7], v[48:49], v[48:49]
	v_pk_fma_f32 v[50:51], v[8:9], v[50:51], v[50:51]
	v_pk_fma_f32 v[20:21], v[10:11], v[20:21], v[20:21]
	v_pk_fma_f32 v[24:25], v[12:13], v[24:25], v[24:25]
	v_pk_fma_f32 v[34:35], v[18:19], v[34:35], v[34:35]
	v_pk_fma_f32 v[26:27], v[36:37], v[26:27], v[26:27]
	v_pk_fma_f32 v[28:29], v[44:45], v[28:29], v[28:29]
	v_rcp_f32_e64 v46, v46 clamp
	v_rcp_f32_e64 v47, v47 clamp
	v_rcp_f32_e64 v48, v48 clamp
	v_rcp_f32_e64 v49, v49 clamp
	v_rcp_f32_e64 v50, v50 clamp
	v_rcp_f32_e64 v51, v51 clamp
	v_rcp_f32_e64 v20, v20 clamp
	v_rcp_f32_e64 v21, v21 clamp
	v_rcp_f32_e64 v24, v24 clamp
	v_rcp_f32_e64 v25, v25 clamp
	v_rcp_f32_e64 v34, v34 clamp
	v_rcp_f32_e64 v35, v35 clamp
	v_rcp_f32_e64 v26, v26 clamp
	v_rcp_f32_e64 v27, v27 clamp
	v_rcp_f32_e64 v28, v28 clamp
	v_rcp_f32_e64 v29, v29 clamp
	v_pk_mul_f32 v[46:47], v[58:59], v[46:47]
	v_pk_mul_f32 v[48:49], v[60:61], v[48:49]
	v_pk_mul_f32 v[50:51], v[52:53], v[50:51]
	v_pk_mul_f32 v[20:21], v[22:23], v[20:21]
	v_pk_mul_f32 v[22:23], v[54:55], v[24:25]
	v_pk_mul_f32 v[24:25], v[56:57], v[34:35]
	v_pk_mul_f32 v[26:27], v[30:31], v[26:27]
	v_pk_mul_f32 v[28:29], v[32:33], v[28:29]
	v_pk_fma_f32 v[4:5], v[4:5], v[46:47], v[46:47]
	v_pk_fma_f32 v[6:7], v[6:7], v[48:49], v[48:49]
	v_pk_fma_f32 v[8:9], v[8:9], v[50:51], v[50:51]
	v_pk_fma_f32 v[10:11], v[10:11], v[20:21], v[20:21]
	v_pk_fma_f32 v[12:13], v[12:13], v[22:23], v[22:23]
	v_pk_fma_f32 v[18:19], v[18:19], v[24:25], v[24:25]
	v_pk_fma_f32 v[30:31], v[36:37], v[26:27], v[26:27]
	v_pk_fma_f32 v[32:33], v[44:45], v[28:29], v[28:29]
	s_nop 0
	v_pk_fma_f32 v[4:5], v[4:5], v[4:5], s[4:5] neg_lo:[1,0,0] neg_hi:[1,0,0] clamp
	v_pk_fma_f32 v[6:7], v[6:7], v[6:7], s[4:5] neg_lo:[1,0,0] neg_hi:[1,0,0] clamp
	v_pk_fma_f32 v[8:9], v[8:9], v[8:9], s[4:5] neg_lo:[1,0,0] neg_hi:[1,0,0] clamp
	v_pk_fma_f32 v[10:11], v[10:11], v[10:11], s[4:5] neg_lo:[1,0,0] neg_hi:[1,0,0] clamp
	v_pk_fma_f32 v[12:13], v[12:13], v[12:13], s[4:5] neg_lo:[1,0,0] neg_hi:[1,0,0] clamp
	v_pk_fma_f32 v[18:19], v[18:19], v[18:19], s[4:5] neg_lo:[1,0,0] neg_hi:[1,0,0] clamp
	v_pk_fma_f32 v[30:31], v[30:31], v[30:31], s[4:5] neg_lo:[1,0,0] neg_hi:[1,0,0] clamp
	s_nop 0
	v_pk_fma_f32 v[32:33], v[32:33], v[32:33], s[4:5] neg_lo:[1,0,0] neg_hi:[1,0,0] clamp
	s_nop 0
	v_pk_fma_f32 v[8:9], v[8:9], v[8:9], s[8:9] op_sel_hi:[1,1,0]
	v_pk_fma_f32 v[10:11], v[10:11], v[10:11], s[8:9] op_sel_hi:[1,1,0]
	v_pk_fma_f32 v[12:13], v[12:13], v[12:13], s[8:9] op_sel_hi:[1,1,0]
	v_pk_fma_f32 v[18:19], v[18:19], v[18:19], s[8:9] op_sel_hi:[1,1,0]
	v_pk_fma_f32 v[32:33], v[32:33], v[32:33], s[8:9] op_sel_hi:[1,1,0]
	v_pk_fma_f32 v[4:5], v[4:5], v[4:5], s[8:9] op_sel_hi:[1,1,0]
	v_pk_fma_f32 v[6:7], v[6:7], v[6:7], s[8:9] op_sel_hi:[1,1,0]
	v_pk_fma_f32 v[30:31], v[30:31], v[30:31], s[8:9] op_sel_hi:[1,1,0]
	v_pk_mul_f32 v[8:9], v[50:51], v[8:9]
	v_pk_mul_f32 v[84:85], v[20:21], v[10:11]
	v_pk_mul_f32 v[86:87], v[22:23], v[12:13]
	v_pk_mul_f32 v[10:11], v[24:25], v[18:19]
	v_pk_mul_f32 v[12:13], v[28:29], v[32:33]
	v_pk_mul_f32 v[64:65], v[46:47], v[4:5]
	v_pk_mul_f32 v[82:83], v[48:49], v[6:7]
	v_pk_mul_f32 v[20:21], v[30:31], v[26:27]
	ds_read_b128 v[4:7], v72 offset:6144
	ds_read_b128 v[22:25], v71 offset:42368
	ds_read_b128 v[26:29], v72 offset:7168
	ds_read_b128 v[30:33], v71 offset:42432
	v_cvt_pk_f16_f32 v19, v84, v85
	v_cvt_pk_f16_f32 v18, v8, v9
	v_cvt_pk_f16_f32 v20, v20, v21
	v_cvt_pk_f16_f32 v21, v12, v13
	s_waitcnt lgkmcnt(2)
	v_mfma_f32_16x16x32_f16 v[34:37], v[4:7], v[14:17], v[22:25]
	v_mfma_f32_16x16x32_f16 v[44:47], v[4:7], v[0:3], v[22:25]
	ds_read_b128 v[4:7], v72 offset:8192
	ds_read_b128 v[48:51], v71 offset:42496
	s_waitcnt lgkmcnt(2)
	v_mfma_f32_16x16x32_f16 v[52:55], v[26:29], v[14:17], v[30:33]
	v_cvt_pk_f16_f32 v22, v64, v65
	v_cvt_pk_f16_f32 v23, v82, v83
	v_cvt_pk_f16_f32 v24, v86, v87
	v_mfma_f32_16x16x32_f16 v[26:29], v[26:29], v[0:3], v[30:33]
	ds_read_b128 v[56:59], v71 offset:42560
	v_exp_f32_e32 v86, v34
	v_exp_f32_e32 v87, v35
	ds_read_b128 v[30:33], v72 offset:9216
	s_waitcnt lgkmcnt(2)
	v_mfma_f32_16x16x32_f16 v[60:63], v[4:7], v[14:17], v[48:51]
	v_exp_f32_e64 v88, v52 clamp
	v_exp_f32_e64 v89, v53 clamp
	v_exp_f32_e64 v90, v54 clamp
	v_mfma_f32_16x16x32_f16 v[48:51], v[4:7], v[0:3], v[48:51]
	ds_read_b128 v[64:67], v72 offset:10240
	ds_read_b128 v[74:77], v71 offset:42624
	s_nop 1
	v_exp_f32_e32 v4, v60
	s_waitcnt lgkmcnt(2)
	v_mfma_f32_16x16x32_f16 v[78:81], v[30:33], v[14:17], v[56:59]
	v_exp_f32_e32 v5, v61
	v_exp_f32_e32 v60, v36
	v_exp_f32_e32 v61, v37
	v_mfma_f32_16x16x32_f16 v[30:33], v[30:33], v[0:3], v[56:59]
	ds_read_b128 v[82:85], v71 offset:42688
	v_exp_f32_e64 v91, v55 clamp
	v_exp_f32_e32 v6, v62
	ds_read_b128 v[56:59], v72 offset:11264
	s_waitcnt lgkmcnt(2)
	v_mfma_f32_16x16x32_f16 v[34:37], v[64:67], v[14:17], v[74:77]
	v_exp_f32_e32 v7, v63
	v_exp_f32_e32 v8, v48
	v_exp_f32_e32 v9, v49
	v_mfma_f32_16x16x32_f16 v[52:55], v[64:67], v[0:3], v[74:77]
	v_exp_f32_e32 v44, v44
	v_exp_f32_e32 v45, v45
	v_exp_f32_e64 v26, v26 clamp
	s_waitcnt lgkmcnt(0)
	v_mfma_f32_16x16x32_f16 v[14:17], v[56:59], v[14:17], v[82:85]
	v_exp_f32_e64 v27, v27 clamp
	v_exp_f32_e32 v46, v46
	v_exp_f32_e32 v47, v47
	v_mfma_f32_16x16x32_f16 v[56:59], v[56:59], v[0:3], v[82:85]
	v_exp_f32_e64 v28, v28 clamp
	s_nop 2
	v_exp_f32_e32 v2, v14
	v_exp_f32_e32 v3, v15
	v_exp_f32_e32 v14, v16
	v_exp_f32_e32 v15, v17
	v_exp_f32_e32 v16, v30
	v_exp_f32_e32 v17, v31
	v_exp_f32_e64 v29, v29 clamp
	v_exp_f32_e32 v0, v50
	v_exp_f32_e32 v1, v51
	v_exp_f32_e32 v48, v78
	v_exp_f32_e32 v49, v79
	v_exp_f32_e64 v34, v34 clamp
	v_exp_f32_e64 v35, v35 clamp
	v_exp_f32_e32 v50, v80
	v_exp_f32_e32 v51, v81
	v_exp_f32_e64 v36, v36 clamp
	v_exp_f32_e64 v37, v37 clamp
	v_exp_f32_e64 v30, v52 clamp
	v_exp_f32_e64 v31, v53 clamp
	v_exp_f32_e32 v52, v56
	v_exp_f32_e32 v53, v57
	v_exp_f32_e32 v32, v32
	v_exp_f32_e32 v33, v33
	v_exp_f32_e64 v54, v54 clamp
	v_exp_f32_e64 v55, v55 clamp
	v_exp_f32_e32 v56, v58
	v_cvt_pk_f16_f32 v25, v10, v11
	v_exp_f32_e32 v57, v59
	v_pk_fma_f32 v[30:31], v[30:31], s[2:3], 1.0 op_sel_hi:[1,0,0]
	v_pk_fma_f32 v[10:11], v[88:89], s[2:3], 1.0 op_sel_hi:[1,0,0]
	v_pk_fma_f32 v[12:13], v[90:91], s[2:3], 1.0 op_sel_hi:[1,0,0]
	v_pk_fma_f32 v[26:27], v[26:27], s[2:3], 1.0 op_sel_hi:[1,0,0]
	v_pk_fma_f32 v[28:29], v[28:29], s[2:3], 1.0 op_sel_hi:[1,0,0]
	v_pk_fma_f32 v[34:35], v[34:35], s[2:3], 1.0 op_sel_hi:[1,0,0]
	v_pk_fma_f32 v[36:37], v[36:37], s[2:3], 1.0 op_sel_hi:[1,0,0]
	v_pk_fma_f32 v[54:55], v[54:55], s[2:3], 1.0 op_sel_hi:[1,0,0]
	v_pk_fma_f32 v[16:17], v[16:17], v[30:31], v[30:31]
	v_pk_fma_f32 v[58:59], v[86:87], v[10:11], v[10:11]
	v_pk_fma_f32 v[10:11], v[10:11], s[6:7], v[40:41] op_sel_hi:[1,0,0] neg_lo:[1,0,0] neg_hi:[1,0,0]
	v_pk_fma_f32 v[60:61], v[60:61], v[12:13], v[12:13]
	v_pk_fma_f32 v[12:13], v[12:13], s[6:7], v[40:41] op_sel_hi:[1,0,0] neg_lo:[1,0,0] neg_hi:[1,0,0]
	v_pk_fma_f32 v[44:45], v[44:45], v[26:27], v[26:27]
	v_pk_fma_f32 v[46:47], v[46:47], v[28:29], v[28:29]
	v_pk_fma_f32 v[48:49], v[48:49], v[34:35], v[34:35]
	v_pk_fma_f32 v[50:51], v[50:51], v[36:37], v[36:37]
	v_pk_fma_f32 v[32:33], v[32:33], v[54:55], v[54:55]
	v_pk_fma_f32 v[16:17], v[52:53], v[16:17], v[16:17]
	v_pk_fma_f32 v[26:27], v[26:27], s[6:7], v[40:41] op_sel_hi:[1,0,0] neg_lo:[1,0,0] neg_hi:[1,0,0]
	v_pk_fma_f32 v[28:29], v[28:29], s[6:7], v[40:41] op_sel_hi:[1,0,0] neg_lo:[1,0,0] neg_hi:[1,0,0]
	v_pk_fma_f32 v[34:35], v[34:35], s[6:7], v[40:41] op_sel_hi:[1,0,0] neg_lo:[1,0,0] neg_hi:[1,0,0]
	v_pk_fma_f32 v[36:37], v[36:37], s[6:7], v[40:41] op_sel_hi:[1,0,0] neg_lo:[1,0,0] neg_hi:[1,0,0]
	v_pk_fma_f32 v[30:31], v[30:31], s[6:7], v[40:41] op_sel_hi:[1,0,0] neg_lo:[1,0,0] neg_hi:[1,0,0]
	v_pk_fma_f32 v[54:55], v[54:55], s[6:7], v[40:41] op_sel_hi:[1,0,0] neg_lo:[1,0,0] neg_hi:[1,0,0]
	v_pk_fma_f32 v[58:59], v[4:5], v[58:59], v[58:59]
	v_pk_fma_f32 v[60:61], v[6:7], v[60:61], v[60:61]
	v_pk_fma_f32 v[44:45], v[8:9], v[44:45], v[44:45]
	v_pk_fma_f32 v[46:47], v[0:1], v[46:47], v[46:47]
	v_pk_fma_f32 v[48:49], v[2:3], v[48:49], v[48:49]
	v_pk_fma_f32 v[50:51], v[14:15], v[50:51], v[50:51]
	v_pk_fma_f32 v[32:33], v[56:57], v[32:33], v[32:33]
	v_rcp_f32_e64 v16, v16 clamp
	v_rcp_f32_e64 v17, v17 clamp
	v_rcp_f32_e64 v58, v58 clamp
	v_rcp_f32_e64 v59, v59 clamp
	v_rcp_f32_e64 v60, v60 clamp
	v_rcp_f32_e64 v61, v61 clamp
	v_rcp_f32_e64 v44, v44 clamp
	v_rcp_f32_e64 v45, v45 clamp
	v_rcp_f32_e64 v46, v46 clamp
	v_rcp_f32_e64 v47, v47 clamp
	v_rcp_f32_e64 v48, v48 clamp
	v_rcp_f32_e64 v49, v49 clamp
	v_rcp_f32_e64 v50, v50 clamp
	v_rcp_f32_e64 v51, v51 clamp
	v_rcp_f32_e64 v32, v32 clamp
	v_rcp_f32_e64 v33, v33 clamp
	v_pk_mul_f32 v[10:11], v[10:11], v[58:59]
	v_pk_mul_f32 v[12:13], v[12:13], v[60:61]
	v_pk_mul_f32 v[26:27], v[26:27], v[44:45]
	v_pk_mul_f32 v[34:35], v[34:35], v[48:49]
	v_pk_mul_f32 v[36:37], v[36:37], v[50:51]
	v_pk_mul_f32 v[28:29], v[28:29], v[46:47]
	v_pk_mul_f32 v[16:17], v[30:31], v[16:17]
	v_pk_mul_f32 v[30:31], v[54:55], v[32:33]
	v_pk_fma_f32 v[4:5], v[4:5], v[10:11], v[10:11]
	v_pk_fma_f32 v[6:7], v[6:7], v[12:13], v[12:13]
	v_pk_fma_f32 v[8:9], v[8:9], v[26:27], v[26:27]
	v_pk_fma_f32 v[2:3], v[2:3], v[34:35], v[34:35]
	v_pk_fma_f32 v[14:15], v[14:15], v[36:37], v[36:37]
	v_pk_fma_f32 v[0:1], v[0:1], v[28:29], v[28:29]
	v_pk_fma_f32 v[32:33], v[52:53], v[16:17], v[16:17]
	v_pk_fma_f32 v[44:45], v[56:57], v[30:31], v[30:31]
	s_nop 0
	v_pk_fma_f32 v[4:5], v[4:5], v[4:5], s[4:5] neg_lo:[1,0,0] neg_hi:[1,0,0] clamp
	v_pk_fma_f32 v[6:7], v[6:7], v[6:7], s[4:5] neg_lo:[1,0,0] neg_hi:[1,0,0] clamp
	v_pk_fma_f32 v[8:9], v[8:9], v[8:9], s[4:5] neg_lo:[1,0,0] neg_hi:[1,0,0] clamp
	v_pk_fma_f32 v[0:1], v[0:1], v[0:1], s[4:5] neg_lo:[1,0,0] neg_hi:[1,0,0] clamp
	v_pk_fma_f32 v[2:3], v[2:3], v[2:3], s[4:5] neg_lo:[1,0,0] neg_hi:[1,0,0] clamp
	v_pk_fma_f32 v[14:15], v[14:15], v[14:15], s[4:5] neg_lo:[1,0,0] neg_hi:[1,0,0] clamp
	v_pk_fma_f32 v[32:33], v[32:33], v[32:33], s[4:5] neg_lo:[1,0,0] neg_hi:[1,0,0] clamp
	s_nop 0
	v_pk_fma_f32 v[44:45], v[44:45], v[44:45], s[4:5] neg_lo:[1,0,0] neg_hi:[1,0,0] clamp
	s_nop 0
	v_pk_fma_f32 v[32:33], v[32:33], v[32:33], s[8:9] op_sel_hi:[1,1,0]
	v_pk_fma_f32 v[4:5], v[4:5], v[4:5], s[8:9] op_sel_hi:[1,1,0]
	v_pk_fma_f32 v[6:7], v[6:7], v[6:7], s[8:9] op_sel_hi:[1,1,0]
	v_pk_fma_f32 v[8:9], v[8:9], v[8:9], s[8:9] op_sel_hi:[1,1,0]
	v_pk_fma_f32 v[0:1], v[0:1], v[0:1], s[8:9] op_sel_hi:[1,1,0]
	v_pk_fma_f32 v[2:3], v[2:3], v[2:3], s[8:9] op_sel_hi:[1,1,0]
	v_pk_fma_f32 v[14:15], v[14:15], v[14:15], s[8:9] op_sel_hi:[1,1,0]
	v_pk_fma_f32 v[44:45], v[44:45], v[44:45], s[8:9] op_sel_hi:[1,1,0]
	v_pk_mul_f32 v[16:17], v[32:33], v[16:17]
	v_pk_mul_f32 v[52:53], v[10:11], v[4:5]
	v_pk_mul_f32 v[54:55], v[12:13], v[6:7]
	v_pk_mul_f32 v[26:27], v[26:27], v[8:9]
	v_pk_mul_f32 v[28:29], v[28:29], v[0:1]
	v_pk_mul_f32 v[56:57], v[34:35], v[2:3]
	v_pk_mul_f32 v[58:59], v[36:37], v[14:15]
	v_pk_mul_f32 v[60:61], v[30:31], v[44:45]
	ds_read_b128 v[0:3], v72 offset:12288
	ds_read_b128 v[4:7], v71 offset:42752
	ds_read_b128 v[8:11], v72 offset:13312
	ds_read_b128 v[12:15], v72 offset:14336
	ds_read_b128 v[34:37], v72 offset:15360
	ds_read_b128 v[44:47], v71 offset:42816
	v_cvt_pk_f16_f32 v30, v52, v53
	v_cvt_pk_f16_f32 v26, v26, v27
	v_cvt_pk_f16_f32 v31, v54, v55
	s_waitcnt lgkmcnt(4)
	v_mfma_f32_16x16x32_f16 v[48:51], v[0:3], v[22:25], v[4:7]
	v_cvt_pk_f16_f32 v32, v56, v57
	v_cvt_pk_f16_f32 v33, v58, v59
	v_cvt_pk_f16_f32 v27, v28, v29
	v_mfma_f32_16x16x32_f16 v[0:3], v[0:3], v[18:21], v[4:7]
	v_cvt_pk_f16_f32 v28, v16, v17
	v_cvt_pk_f16_f32 v29, v60, v61
	s_add_i32 s11, s9, s12
	s_waitcnt lgkmcnt(3)
	v_mfma_f32_16x16x32_f16 v[48:51], v[8:11], v[30:33], v[48:51]
	s_cmp_lt_i32 s11, 0x8000
	s_cselect_b32 s10, s11, s10
	s_ashr_i32 s11, s10, 31
	v_mfma_f32_16x16x32_f16 v[52:55], v[8:11], v[26:29], v[0:3]
	ds_read_b128 v[4:7], v72 offset:17408
	ds_read_b128 v[8:11], v71 offset:42880
	s_lshl_b64 s[10:11], s[10:11], 12
	s_add_u32 s10, s10, s36
	s_addc_u32 s11, s11, s37
	ds_read_b128 v[0:3], v72 offset:16384
	s_waitcnt lgkmcnt(3)
	v_mfma_f32_16x16x32_f16 v[56:59], v[12:15], v[22:25], v[44:47]
	v_exp_f32_e32 v106, v48
	v_exp_f32_e32 v107, v49
	v_exp_f32_e32 v110, v50
	v_mfma_f32_16x16x32_f16 v[12:15], v[12:15], v[18:21], v[44:47]
	v_exp_f32_e32 v111, v51
	v_exp_f32_e32 v114, v52
	v_exp_f32_e32 v115, v53
	v_mfma_f32_16x16x32_f16 v[44:47], v[34:37], v[30:33], v[56:59]
	v_mfma_f32_16x16x32_f16 v[56:59], v[34:37], v[26:29], v[12:15]
	ds_read_b128 v[34:37], v72 offset:19456
	ds_read_b128 v[60:63], v71 offset:42944
	s_nop 4
	v_exp_f32_e64 v108, v44 clamp
	ds_read_b128 v[12:15], v72 offset:18432
	s_waitcnt lgkmcnt(3)
	v_mfma_f32_16x16x32_f16 v[64:67], v[0:3], v[22:25], v[8:11]
	v_exp_f32_e64 v109, v45 clamp
	v_exp_f32_e64 v112, v46 clamp
	v_exp_f32_e64 v113, v47 clamp
	v_mfma_f32_16x16x32_f16 v[0:3], v[0:3], v[18:21], v[8:11]
	v_exp_f32_e64 v116, v56 clamp
	v_exp_f32_e64 v117, v57 clamp
	v_exp_f32_e64 v58, v58 clamp
	v_mfma_f32_16x16x32_f16 v[64:67], v[4:7], v[30:33], v[64:67]
	v_exp_f32_e64 v59, v59 clamp
	v_mfma_f32_16x16x32_f16 v[74:77], v[4:7], v[26:29], v[0:3]
	ds_read_b128 v[78:81], v72 offset:20480
	ds_read_b128 v[82:85], v72 offset:21504
	ds_read_b128 v[86:89], v71 offset:43008
	s_waitcnt lgkmcnt(3)
	v_mfma_f32_16x16x32_f16 v[6:9], v[12:15], v[22:25], v[60:63]
	v_mfma_f32_16x16x32_f16 v[60:63], v[12:15], v[18:21], v[60:63]
	global_load_dwordx4 v[10:13], v39, s[10:11] offset:16
	global_load_dwordx4 v[14:17], v39, s[10:11]
	global_load_dwordx4 v[2:5], v39, s[10:11] offset:2064
	v_mfma_f32_16x16x32_f16 v[90:93], v[34:37], v[30:33], v[6:9]
	v_mfma_f32_16x16x32_f16 v[60:63], v[34:37], v[26:29], v[60:63]
	s_nop 1
	global_load_dwordx4 v[6:9], v39, s[10:11] offset:2048
	ds_read_b128 v[94:97], v72 offset:22528
	ds_read_b128 v[98:101], v72 offset:23552
	ds_read_b128 v[102:105], v71 offset:43072
	s_waitcnt lgkmcnt(3)
	v_mfma_f32_16x16x32_f16 v[44:47], v[78:81], v[22:25], v[86:89]
	v_exp_f32_e32 v0, v64
	v_exp_f32_e32 v1, v65
	v_exp_f32_e32 v34, v66
	v_mfma_f32_16x16x32_f16 v[48:51], v[78:81], v[18:21], v[86:89]
	v_exp_f32_e32 v35, v67
	v_exp_f32_e32 v36, v74
	v_exp_f32_e32 v37, v75
	v_mfma_f32_16x16x32_f16 v[64:67], v[82:85], v[30:33], v[44:47]
	v_exp_f32_e32 v74, v54
	v_exp_f32_e32 v75, v55
	v_exp_f32_e32 v78, v92
	v_mfma_f32_16x16x32_f16 v[50:53], v[82:85], v[26:29], v[48:51]
	v_exp_f32_e32 v44, v76
	v_exp_f32_e32 v45, v77
	v_exp_f32_e32 v76, v90
	s_waitcnt lgkmcnt(0)
	v_mfma_f32_16x16x32_f16 v[46:49], v[94:97], v[22:25], v[102:105]
	v_exp_f32_e32 v77, v91
	v_exp_f32_e64 v64, v64 clamp
	v_exp_f32_e64 v65, v65 clamp
	v_mfma_f32_16x16x32_f16 v[54:57], v[94:97], v[18:21], v[102:105]
	v_exp_f32_e32 v79, v93
	v_exp_f32_e64 v66, v66 clamp
	v_exp_f32_e64 v67, v67 clamp
	v_mfma_f32_16x16x32_f16 v[46:49], v[98:101], v[30:33], v[46:49]
	v_exp_f32_e32 v60, v60
	v_exp_f32_e32 v61, v61
	v_exp_f32_e64 v50, v50 clamp
	v_mfma_f32_16x16x32_f16 v[54:57], v[98:101], v[26:29], v[54:57]
	v_exp_f32_e64 v51, v51 clamp
	s_nop 2
	v_exp_f32_e32 v46, v46
	v_exp_f32_e32 v47, v47
	v_exp_f32_e32 v48, v48
	v_exp_f32_e32 v49, v49
	v_exp_f32_e32 v54, v54
	v_exp_f32_e32 v55, v55
	v_exp_f32_e32 v62, v62
	v_exp_f32_e32 v63, v63
	v_exp_f32_e64 v52, v52 clamp
	v_exp_f32_e64 v53, v53 clamp
	v_exp_f32_e32 v56, v56
	v_exp_f32_e32 v57, v57
	v_pk_fma_f32 v[80:81], v[108:109], s[2:3], 1.0 op_sel_hi:[1,0,0]
	v_pk_fma_f32 v[82:83], v[112:113], s[2:3], 1.0 op_sel_hi:[1,0,0]
	v_pk_fma_f32 v[84:85], v[116:117], s[2:3], 1.0 op_sel_hi:[1,0,0]
	v_pk_fma_f32 v[58:59], v[58:59], s[2:3], 1.0 op_sel_hi:[1,0,0]
	v_pk_fma_f32 v[64:65], v[64:65], s[2:3], 1.0 op_sel_hi:[1,0,0]
	v_pk_fma_f32 v[66:67], v[66:67], s[2:3], 1.0 op_sel_hi:[1,0,0]
	v_pk_fma_f32 v[50:51], v[50:51], s[2:3], 1.0 op_sel_hi:[1,0,0]
	v_pk_fma_f32 v[52:53], v[52:53], s[2:3], 1.0 op_sel_hi:[1,0,0]
	v_pk_fma_f32 v[86:87], v[106:107], v[80:81], v[80:81]
	v_pk_fma_f32 v[88:89], v[110:111], v[82:83], v[82:83]
	v_pk_fma_f32 v[90:91], v[114:115], v[84:85], v[84:85]
	v_pk_fma_f32 v[74:75], v[74:75], v[58:59], v[58:59]
	v_pk_fma_f32 v[76:77], v[76:77], v[64:65], v[64:65]
	v_pk_fma_f32 v[78:79], v[78:79], v[66:67], v[66:67]
	v_pk_fma_f32 v[60:61], v[60:61], v[50:51], v[50:51]
	v_pk_fma_f32 v[62:63], v[62:63], v[52:53], v[52:53]
	v_pk_fma_f32 v[80:81], v[80:81], s[6:7], v[40:41] op_sel_hi:[1,0,0] neg_lo:[1,0,0] neg_hi:[1,0,0]
	v_pk_fma_f32 v[82:83], v[82:83], s[6:7], v[40:41] op_sel_hi:[1,0,0] neg_lo:[1,0,0] neg_hi:[1,0,0]
	v_pk_fma_f32 v[84:85], v[84:85], s[6:7], v[40:41] op_sel_hi:[1,0,0] neg_lo:[1,0,0] neg_hi:[1,0,0]
	v_pk_fma_f32 v[58:59], v[58:59], s[6:7], v[40:41] op_sel_hi:[1,0,0] neg_lo:[1,0,0] neg_hi:[1,0,0]
	v_pk_fma_f32 v[64:65], v[64:65], s[6:7], v[40:41] op_sel_hi:[1,0,0] neg_lo:[1,0,0] neg_hi:[1,0,0]
	v_pk_fma_f32 v[66:67], v[66:67], s[6:7], v[40:41] op_sel_hi:[1,0,0] neg_lo:[1,0,0] neg_hi:[1,0,0]
	v_pk_fma_f32 v[50:51], v[50:51], s[6:7], v[40:41] op_sel_hi:[1,0,0] neg_lo:[1,0,0] neg_hi:[1,0,0]
	v_pk_fma_f32 v[52:53], v[52:53], s[6:7], v[40:41] op_sel_hi:[1,0,0] neg_lo:[1,0,0] neg_hi:[1,0,0]
	v_pk_fma_f32 v[86:87], v[0:1], v[86:87], v[86:87]
	v_pk_fma_f32 v[88:89], v[34:35], v[88:89], v[88:89]
	v_pk_fma_f32 v[90:91], v[36:37], v[90:91], v[90:91]
	v_pk_fma_f32 v[74:75], v[44:45], v[74:75], v[74:75]
	v_pk_fma_f32 v[76:77], v[46:47], v[76:77], v[76:77]
	v_pk_fma_f32 v[78:79], v[48:49], v[78:79], v[78:79]
	v_pk_fma_f32 v[60:61], v[54:55], v[60:61], v[60:61]
	v_pk_fma_f32 v[62:63], v[56:57], v[62:63], v[62:63]
	v_rcp_f32_e64 v86, v86 clamp
	v_rcp_f32_e64 v87, v87 clamp
	v_rcp_f32_e64 v88, v88 clamp
	v_rcp_f32_e64 v89, v89 clamp
	v_rcp_f32_e64 v90, v90 clamp
	v_rcp_f32_e64 v91, v91 clamp
	v_rcp_f32_e64 v74, v74 clamp
	v_rcp_f32_e64 v75, v75 clamp
	v_rcp_f32_e64 v76, v76 clamp
	v_rcp_f32_e64 v77, v77 clamp
	v_rcp_f32_e64 v78, v78 clamp
	v_rcp_f32_e64 v79, v79 clamp
	v_rcp_f32_e64 v60, v60 clamp
	v_rcp_f32_e64 v61, v61 clamp
	v_rcp_f32_e64 v62, v62 clamp
	v_rcp_f32_e64 v63, v63 clamp
	v_pk_mul_f32 v[80:81], v[80:81], v[86:87]
	v_pk_mul_f32 v[82:83], v[82:83], v[88:89]
	v_pk_mul_f32 v[84:85], v[84:85], v[90:91]
	v_pk_mul_f32 v[58:59], v[58:59], v[74:75]
	v_pk_mul_f32 v[64:65], v[64:65], v[76:77]
	v_pk_mul_f32 v[66:67], v[66:67], v[78:79]
	v_pk_mul_f32 v[50:51], v[50:51], v[60:61]
	v_pk_mul_f32 v[60:61], v[52:53], v[62:63]
	v_pk_fma_f32 v[0:1], v[0:1], v[80:81], v[80:81]
	v_pk_fma_f32 v[34:35], v[34:35], v[82:83], v[82:83]
	v_pk_fma_f32 v[36:37], v[36:37], v[84:85], v[84:85]
	v_pk_fma_f32 v[44:45], v[44:45], v[58:59], v[58:59]
	v_pk_fma_f32 v[46:47], v[46:47], v[64:65], v[64:65]
	v_pk_fma_f32 v[48:49], v[48:49], v[66:67], v[66:67]
	v_pk_fma_f32 v[52:53], v[54:55], v[50:51], v[50:51]
	v_pk_fma_f32 v[54:55], v[56:57], v[60:61], v[60:61]
	s_nop 0
	v_pk_fma_f32 v[0:1], v[0:1], v[0:1], s[4:5] neg_lo:[1,0,0] neg_hi:[1,0,0] clamp
	v_pk_fma_f32 v[34:35], v[34:35], v[34:35], s[4:5] neg_lo:[1,0,0] neg_hi:[1,0,0] clamp
	v_pk_fma_f32 v[36:37], v[36:37], v[36:37], s[4:5] neg_lo:[1,0,0] neg_hi:[1,0,0] clamp
	v_pk_fma_f32 v[44:45], v[44:45], v[44:45], s[4:5] neg_lo:[1,0,0] neg_hi:[1,0,0] clamp
	v_pk_fma_f32 v[46:47], v[46:47], v[46:47], s[4:5] neg_lo:[1,0,0] neg_hi:[1,0,0] clamp
	v_pk_fma_f32 v[48:49], v[48:49], v[48:49], s[4:5] neg_lo:[1,0,0] neg_hi:[1,0,0] clamp
	v_pk_fma_f32 v[52:53], v[52:53], v[52:53], s[4:5] neg_lo:[1,0,0] neg_hi:[1,0,0] clamp
	s_nop 0
	v_pk_fma_f32 v[54:55], v[54:55], v[54:55], s[4:5] neg_lo:[1,0,0] neg_hi:[1,0,0] clamp
	s_nop 0
	v_pk_fma_f32 v[0:1], v[0:1], v[0:1], s[8:9] op_sel_hi:[1,1,0]
	v_pk_fma_f32 v[56:57], v[34:35], v[34:35], s[8:9] op_sel_hi:[1,1,0]
	v_pk_fma_f32 v[36:37], v[36:37], v[36:37], s[8:9] op_sel_hi:[1,1,0]
	v_pk_fma_f32 v[44:45], v[44:45], v[44:45], s[8:9] op_sel_hi:[1,1,0]
	v_pk_fma_f32 v[46:47], v[46:47], v[46:47], s[8:9] op_sel_hi:[1,1,0]
	v_pk_fma_f32 v[48:49], v[48:49], v[48:49], s[8:9] op_sel_hi:[1,1,0]
	v_pk_fma_f32 v[62:63], v[52:53], v[52:53], s[8:9] op_sel_hi:[1,1,0]
	v_pk_fma_f32 v[74:75], v[54:55], v[54:55], s[8:9] op_sel_hi:[1,1,0]
	v_pk_mul_f32 v[34:35], v[80:81], v[0:1]
	v_pk_mul_f32 v[56:57], v[82:83], v[56:57]
	v_pk_mul_f32 v[36:37], v[84:85], v[36:37]
	v_pk_mul_f32 v[52:53], v[58:59], v[44:45]
	v_pk_mul_f32 v[54:55], v[64:65], v[46:47]
	v_pk_mul_f32 v[0:1], v[66:67], v[48:49]
	v_pk_mul_f32 v[46:47], v[62:63], v[50:51]
	v_pk_mul_f32 v[44:45], v[60:61], v[74:75]
	ds_read_b128 v[48:51], v72 offset:24576
	ds_read_b128 v[58:61], v71 offset:43136
	ds_read_b128 v[62:65], v72 offset:25600
	ds_read_b128 v[74:77], v72 offset:26624
	ds_read_b128 v[78:81], v72 offset:27648
	ds_read_b128 v[82:85], v71 offset:43200
	v_cvt_pk_f16_f32 v34, v34, v35
	v_cvt_pk_f16_f32 v35, v56, v57
	s_waitcnt lgkmcnt(4)
	v_mfma_f32_16x16x32_f16 v[86:89], v[48:51], v[22:25], v[58:61]
	v_mfma_f32_16x16x32_f16 v[48:51], v[48:51], v[18:21], v[58:61]
	s_waitcnt lgkmcnt(3)
	v_mfma_f32_16x16x32_f16 v[58:61], v[62:65], v[30:33], v[86:89]
	v_mfma_f32_16x16x32_f16 v[86:89], v[62:65], v[26:29], v[48:51]
	ds_read_b128 v[62:65], v72 offset:29696
	ds_read_b128 v[90:93], v71 offset:43264
	s_nop 2
	ds_read_b128 v[48:51], v72 offset:28672
	s_waitcnt lgkmcnt(3)
	v_mfma_f32_16x16x32_f16 v[94:97], v[74:77], v[22:25], v[82:85]
	v_exp_f32_e32 v120, v86
	v_exp_f32_e32 v121, v87
	v_exp_f32_e32 v122, v88
	v_mfma_f32_16x16x32_f16 v[74:77], v[74:77], v[18:21], v[82:85]
	v_exp_f32_e32 v123, v89
	v_mfma_f32_16x16x32_f16 v[82:85], v[78:81], v[30:33], v[94:97]
	v_mfma_f32_16x16x32_f16 v[74:77], v[78:81], v[26:29], v[74:77]
	ds_read_b128 v[78:81], v72 offset:30720
	s_nop 0
	ds_read_b128 v[94:97], v72 offset:31744
	ds_read_b128 v[98:101], v71 offset:43328
	s_waitcnt lgkmcnt(3)
	v_mfma_f32_16x16x32_f16 v[102:105], v[48:51], v[22:25], v[90:93]
	s_nop 0
	v_exp_f32_e64 v66, v82 clamp
	v_exp_f32_e64 v67, v83 clamp
	v_exp_f32_e64 v118, v84 clamp
	v_mfma_f32_16x16x32_f16 v[48:51], v[48:51], v[18:21], v[90:93]
	v_exp_f32_e64 v119, v85 clamp
	v_exp_f32_e64 v124, v74 clamp
	v_exp_f32_e64 v125, v75 clamp
	v_mfma_f32_16x16x32_f16 v[90:93], v[62:65], v[30:33], v[102:105]
	v_exp_f32_e64 v126, v76 clamp
	v_exp_f32_e64 v127, v77 clamp
	v_mfma_f32_16x16x32_f16 v[102:105], v[62:65], v[26:29], v[48:51]
	ds_read_b128 v[106:109], v72 offset:32768
	ds_read_b128 v[110:113], v72 offset:33792
	v_exp_f32_e32 v62, v58
	v_exp_f32_e32 v63, v59
	v_exp_f32_e32 v64, v60
	v_exp_f32_e32 v65, v61
	ds_read_b128 v[114:117], v71 offset:43392
	s_waitcnt lgkmcnt(3)
	v_mfma_f32_16x16x32_f16 v[58:61], v[78:81], v[22:25], v[98:101]
	v_exp_f32_e32 v48, v90
	v_exp_f32_e32 v49, v91
	v_exp_f32_e32 v50, v92
	v_mfma_f32_16x16x32_f16 v[78:81], v[78:81], v[18:21], v[98:101]
	v_exp_f32_e32 v51, v93
	v_mfma_f32_16x16x32_f16 v[82:85], v[94:97], v[30:33], v[58:61]
	v_mfma_f32_16x16x32_f16 v[78:81], v[94:97], v[26:29], v[78:81]
	ds_read_b128 v[86:89], v72 offset:34816
	ds_read_b128 v[90:93], v72 offset:35840
	ds_read_b128 v[94:97], v71 offset:43456
	s_waitcnt lgkmcnt(3)
	v_mfma_f32_16x16x32_f16 v[74:77], v[106:109], v[22:25], v[114:117]
	v_exp_f32_e32 v58, v102
	v_exp_f32_e32 v59, v103
	v_exp_f32_e32 v60, v104
	v_mfma_f32_16x16x32_f16 v[98:101], v[106:109], v[18:21], v[114:117]
	v_exp_f32_e32 v61, v105
	v_exp_f32_e32 v102, v82
	v_exp_f32_e32 v103, v83
	v_exp_f32_e32 v104, v84
	v_exp_f32_e32 v105, v85
	v_mfma_f32_16x16x32_f16 v[74:77], v[110:113], v[30:33], v[74:77]
	v_mfma_f32_16x16x32_f16 v[82:85], v[110:113], v[26:29], v[98:101]
	s_waitcnt lgkmcnt(0)
	v_mfma_f32_16x16x32_f16 v[18:21], v[86:89], v[18:21], v[94:97]
	s_nop 4
	v_exp_f32_e64 v106, v74 clamp
	v_exp_f32_e64 v107, v75 clamp
	v_exp_f32_e64 v108, v76 clamp
	v_exp_f32_e64 v109, v77 clamp
	v_mfma_f32_16x16x32_f16 v[74:77], v[86:89], v[22:25], v[94:97]
	v_cvt_pk_f16_f32 v22, v36, v37
	v_cvt_pk_f16_f32 v23, v52, v53
	v_cvt_pk_f16_f32 v36, v54, v55
	v_mfma_f32_16x16x32_f16 v[18:21], v[90:93], v[26:29], v[18:21]
	v_exp_f32_e32 v52, v78
	v_exp_f32_e32 v53, v79
	v_exp_f32_e64 v54, v82 clamp
	v_mfma_f32_16x16x32_f16 v[30:33], v[90:93], v[30:33], v[74:77]
	v_exp_f32_e64 v55, v83 clamp
	s_nop 2
	v_exp_f32_e32 v18, v18
	v_exp_f32_e32 v19, v19
	v_exp_f32_e32 v26, v80
	v_exp_f32_e32 v27, v81
	v_exp_f32_e32 v30, v30
	v_exp_f32_e32 v31, v31
	v_exp_f32_e32 v32, v32
	v_exp_f32_e32 v33, v33
	v_exp_f32_e64 v28, v84 clamp
	v_exp_f32_e64 v29, v85 clamp
	v_exp_f32_e32 v20, v20
	v_cvt_pk_f16_f32 v24, v46, v47
	v_cvt_pk_f16_f32 v37, v0, v1
	v_cvt_pk_f16_f32 v25, v44, v45
	v_exp_f32_e32 v21, v21
	v_pk_fma_f32 v[0:1], v[66:67], s[2:3], 1.0 op_sel_hi:[1,0,0]
	v_pk_fma_f32 v[44:45], v[118:119], s[2:3], 1.0 op_sel_hi:[1,0,0]
	v_pk_fma_f32 v[46:47], v[124:125], s[2:3], 1.0 op_sel_hi:[1,0,0]
	v_pk_fma_f32 v[56:57], v[126:127], s[2:3], 1.0 op_sel_hi:[1,0,0]
	v_pk_fma_f32 v[66:67], v[106:107], s[2:3], 1.0 op_sel_hi:[1,0,0]
	v_pk_fma_f32 v[74:75], v[108:109], s[2:3], 1.0 op_sel_hi:[1,0,0]
	v_pk_fma_f32 v[54:55], v[54:55], s[2:3], 1.0 op_sel_hi:[1,0,0]
	v_pk_fma_f32 v[28:29], v[28:29], s[2:3], 1.0 op_sel_hi:[1,0,0]
	v_pk_fma_f32 v[62:63], v[62:63], v[0:1], v[0:1]
	v_pk_fma_f32 v[64:65], v[64:65], v[44:45], v[44:45]
	v_pk_fma_f32 v[76:77], v[120:121], v[46:47], v[46:47]
	v_pk_fma_f32 v[78:79], v[122:123], v[56:57], v[56:57]
	v_pk_fma_f32 v[80:81], v[102:103], v[66:67], v[66:67]
	v_pk_fma_f32 v[82:83], v[104:105], v[74:75], v[74:75]
	v_pk_fma_f32 v[52:53], v[52:53], v[54:55], v[54:55]
	v_pk_fma_f32 v[26:27], v[26:27], v[28:29], v[28:29]
	v_pk_fma_f32 v[0:1], v[0:1], s[6:7], v[40:41] op_sel_hi:[1,0,0] neg_lo:[1,0,0] neg_hi:[1,0,0]
	v_pk_fma_f32 v[44:45], v[44:45], s[6:7], v[40:41] op_sel_hi:[1,0,0] neg_lo:[1,0,0] neg_hi:[1,0,0]
	v_pk_fma_f32 v[46:47], v[46:47], s[6:7], v[40:41] op_sel_hi:[1,0,0] neg_lo:[1,0,0] neg_hi:[1,0,0]
	v_pk_fma_f32 v[56:57], v[56:57], s[6:7], v[40:41] op_sel_hi:[1,0,0] neg_lo:[1,0,0] neg_hi:[1,0,0]
	v_pk_fma_f32 v[66:67], v[66:67], s[6:7], v[40:41] op_sel_hi:[1,0,0] neg_lo:[1,0,0] neg_hi:[1,0,0]
	v_pk_fma_f32 v[74:75], v[74:75], s[6:7], v[40:41] op_sel_hi:[1,0,0] neg_lo:[1,0,0] neg_hi:[1,0,0]
	v_pk_fma_f32 v[54:55], v[54:55], s[6:7], v[40:41] op_sel_hi:[1,0,0] neg_lo:[1,0,0] neg_hi:[1,0,0]
	v_pk_fma_f32 v[28:29], v[28:29], s[6:7], v[40:41] op_sel_hi:[1,0,0] neg_lo:[1,0,0] neg_hi:[1,0,0]
	v_pk_fma_f32 v[62:63], v[48:49], v[62:63], v[62:63]
	v_pk_fma_f32 v[64:65], v[50:51], v[64:65], v[64:65]
	v_pk_fma_f32 v[76:77], v[58:59], v[76:77], v[76:77]
	v_pk_fma_f32 v[78:79], v[60:61], v[78:79], v[78:79]
	v_pk_fma_f32 v[80:81], v[30:31], v[80:81], v[80:81]
	v_pk_fma_f32 v[82:83], v[32:33], v[82:83], v[82:83]
	v_pk_fma_f32 v[52:53], v[18:19], v[52:53], v[52:53]
	v_pk_fma_f32 v[26:27], v[20:21], v[26:27], v[26:27]
	v_rcp_f32_e64 v62, v62 clamp
	v_rcp_f32_e64 v63, v63 clamp
	v_rcp_f32_e64 v64, v64 clamp
	v_rcp_f32_e64 v65, v65 clamp
	v_rcp_f32_e64 v76, v76 clamp
	v_rcp_f32_e64 v77, v77 clamp
	v_rcp_f32_e64 v78, v78 clamp
	v_rcp_f32_e64 v79, v79 clamp
	v_rcp_f32_e64 v80, v80 clamp
	v_rcp_f32_e64 v81, v81 clamp
	v_rcp_f32_e64 v82, v82 clamp
	v_rcp_f32_e64 v83, v83 clamp
	v_rcp_f32_e64 v52, v52 clamp
	v_rcp_f32_e64 v53, v53 clamp
	v_rcp_f32_e64 v26, v26 clamp
	v_rcp_f32_e64 v27, v27 clamp
	v_pk_mul_f32 v[52:53], v[54:55], v[52:53]
	v_pk_mul_f32 v[0:1], v[0:1], v[62:63]
	v_pk_mul_f32 v[44:45], v[44:45], v[64:65]
	v_pk_mul_f32 v[46:47], v[46:47], v[76:77]
	v_pk_mul_f32 v[56:57], v[56:57], v[78:79]
	v_pk_mul_f32 v[62:63], v[66:67], v[80:81]
	v_pk_mul_f32 v[64:65], v[74:75], v[82:83]
	v_pk_mul_f32 v[26:27], v[28:29], v[26:27]
	v_pk_fma_f32 v[18:19], v[18:19], v[52:53], v[52:53]
	v_pk_fma_f32 v[28:29], v[48:49], v[0:1], v[0:1]
	v_pk_fma_f32 v[48:49], v[50:51], v[44:45], v[44:45]
	v_pk_fma_f32 v[50:51], v[58:59], v[46:47], v[46:47]
	v_pk_fma_f32 v[54:55], v[60:61], v[56:57], v[56:57]
	v_pk_fma_f32 v[30:31], v[30:31], v[62:63], v[62:63]
	v_pk_fma_f32 v[32:33], v[32:33], v[64:65], v[64:65]
	v_pk_fma_f32 v[20:21], v[20:21], v[26:27], v[26:27]
	s_nop 0
	v_pk_fma_f32 v[28:29], v[28:29], v[28:29], s[4:5] neg_lo:[1,0,0] neg_hi:[1,0,0] clamp
	v_pk_fma_f32 v[48:49], v[48:49], v[48:49], s[4:5] neg_lo:[1,0,0] neg_hi:[1,0,0] clamp
	v_pk_fma_f32 v[50:51], v[50:51], v[50:51], s[4:5] neg_lo:[1,0,0] neg_hi:[1,0,0] clamp
	v_pk_fma_f32 v[54:55], v[54:55], v[54:55], s[4:5] neg_lo:[1,0,0] neg_hi:[1,0,0] clamp
	v_pk_fma_f32 v[30:31], v[30:31], v[30:31], s[4:5] neg_lo:[1,0,0] neg_hi:[1,0,0] clamp
	v_pk_fma_f32 v[32:33], v[32:33], v[32:33], s[4:5] neg_lo:[1,0,0] neg_hi:[1,0,0] clamp
	v_pk_fma_f32 v[18:19], v[18:19], v[18:19], s[4:5] neg_lo:[1,0,0] neg_hi:[1,0,0] clamp
	s_nop 0
	v_pk_fma_f32 v[20:21], v[20:21], v[20:21], s[4:5] neg_lo:[1,0,0] neg_hi:[1,0,0] clamp
	s_nop 0
	v_pk_fma_f32 v[28:29], v[28:29], v[28:29], s[8:9] op_sel_hi:[1,1,0]
	v_pk_fma_f32 v[48:49], v[48:49], v[48:49], s[8:9] op_sel_hi:[1,1,0]
	v_pk_fma_f32 v[50:51], v[50:51], v[50:51], s[8:9] op_sel_hi:[1,1,0]
	v_pk_fma_f32 v[54:55], v[54:55], v[54:55], s[8:9] op_sel_hi:[1,1,0]
	v_pk_fma_f32 v[30:31], v[30:31], v[30:31], s[8:9] op_sel_hi:[1,1,0]
	v_pk_fma_f32 v[32:33], v[32:33], v[32:33], s[8:9] op_sel_hi:[1,1,0]
	v_pk_fma_f32 v[18:19], v[18:19], v[18:19], s[8:9] op_sel_hi:[1,1,0]
	v_pk_fma_f32 v[20:21], v[20:21], v[20:21], s[8:9] op_sel_hi:[1,1,0]
	v_pk_mul_f32 v[0:1], v[0:1], v[28:29]
	v_pk_mul_f32 v[58:59], v[44:45], v[48:49]
	v_pk_mul_f32 v[60:61], v[46:47], v[50:51]
	v_pk_mul_f32 v[54:55], v[56:57], v[54:55]
	v_pk_mul_f32 v[62:63], v[62:63], v[30:31]
	v_pk_mul_f32 v[64:65], v[64:65], v[32:33]
	v_pk_mul_f32 v[66:67], v[18:19], v[52:53]
	v_pk_mul_f32 v[74:75], v[26:27], v[20:21]
	ds_read_b128 v[18:21], v72 offset:36864
	ds_read_b128 v[30:33], v72 offset:37888
	ds_read_b128 v[26:29], v71 offset:43520
	v_cvt_pk_f16_f32 v56, v60, v61
	v_cvt_pk_f16_f32 v57, v54, v55
	v_cvt_pk_f16_f32 v54, v62, v63
	ds_read_b128 v[60:63], v71 offset:43584
	v_cvt_pk_f16_f32 v52, v0, v1
	v_cvt_pk_f16_f32 v53, v58, v59
	s_waitcnt lgkmcnt(1)
	v_mfma_f32_16x16x32_f16 v[48:51], v[18:21], v[34:37], v[26:29]
	v_cvt_pk_f16_f32 v55, v64, v65
	v_cvt_pk_f16_f32 v58, v66, v67
	v_cvt_pk_f16_f32 v59, v74, v75
	v_mfma_f32_16x16x32_f16 v[18:21], v[18:21], v[22:25], v[26:29]
	ds_read_b128 v[44:47], v72 offset:40960
	s_add_i32 s12, s12, s3
	s_add_i32 s10, s20, s12
	v_mfma_f32_16x16x32_f16 v[26:29], v[30:33], v[52:55], v[48:51]
	s_cmp_lt_i32 s10, 0x8000
	v_add_u32_e32 v38, s7, v38
	s_nop 0
	ds_read_b128 v[48:51], v72 offset:38912
	v_mfma_f32_16x16x32_f16 v[18:21], v[30:33], v[56:59], v[18:21]
	ds_read_b128 v[30:33], v72 offset:39936
	s_nop 1
	v_cvt_pk_f16_f32 v1, v28, v29
	v_cvt_pk_f16_f32 v0, v26, v27
	s_waitcnt lgkmcnt(1)
	v_mfma_f32_16x16x32_f16 v[34:37], v[48:51], v[34:37], v[60:63]
	v_pk_max_f16 v27, v1, 0
	v_cvt_pk_f16_f32 v1, v20, v21
	v_pk_max_f16 v26, v0, 0
	v_mfma_f32_16x16x32_f16 v[20:23], v[48:51], v[22:25], v[60:63]
	v_cvt_pk_f16_f32 v0, v18, v19
	v_pk_max_f16 v18, v0, 0
	v_pk_max_f16 v19, v1, 0
	s_waitcnt lgkmcnt(0)
	v_mfma_f32_16x16x32_f16 v[34:37], v[30:33], v[52:55], v[34:37]
	v_mfma_f32_16x16x32_f16 v[20:23], v[30:33], v[56:59], v[20:23]
	s_nop 6
	v_cvt_pk_f16_f32 v0, v34, v35
	v_cvt_pk_f16_f32 v1, v36, v37
	v_pk_max_f16 v28, v0, 0
	v_pk_max_f16 v29, v1, 0
	v_cvt_pk_f16_f32 v0, v20, v21
	v_cvt_pk_f16_f32 v1, v22, v23
	v_pk_max_f16 v20, v0, 0
	v_pk_max_f16 v21, v1, 0
	v_mfma_f32_16x16x32_f16 v[24:27], v[44:47], v[26:29], 0
	s_nop 0
	v_mfma_f32_16x16x32_f16 v[18:21], v[44:47], v[18:21], 0
	s_nop 7
	v_cndmask_b32_e64 v18, v24, v18, s[0:1]
	s_cbranch_scc0 .LBB0_37
